# NSA: block-bit-only score mask for causally interior sub-tiles; GEMM unit headers wait only for the bias loads; diff queue tickets requested one unit ahead
# speedup vs baseline: 1.0149x; 1.0071x over previous
.LBB0_256:
	s_waitcnt vmcnt(8)
	v_mov_b64_e32 v[54:55], v[46:47]
	v_mov_b64_e32 v[58:59], v[50:51]
	v_mov_b64_e32 v[62:63], v[46:47]
	v_mov_b64_e32 v[66:67], v[50:51]
	v_mov_b64_e32 v[70:71], v[46:47]
	v_mov_b64_e32 v[74:75], v[50:51]
	v_mov_b64_e32 v[78:79], v[46:47]
	v_mov_b64_e32 v[82:83], v[50:51]
	v_mov_b64_e32 v[118:119], v[38:39]
	v_mov_b64_e32 v[122:123], v[42:43]
	v_mov_b64_e32 v[126:127], v[38:39]
	v_mov_b64_e32 v[130:131], v[42:43]
	v_mov_b64_e32 v[134:135], v[38:39]
	v_mov_b64_e32 v[138:139], v[42:43]
	v_mov_b64_e32 v[142:143], v[38:39]
	v_mov_b64_e32 v[146:147], v[42:43]
	v_mov_b64_e32 v[86:87], v[46:47]
	v_mov_b64_e32 v[90:91], v[50:51]
	v_mov_b64_e32 v[94:95], v[46:47]
	v_mov_b64_e32 v[98:99], v[50:51]
	v_mov_b64_e32 v[102:103], v[46:47]
	v_mov_b64_e32 v[106:107], v[50:51]
	v_mov_b64_e32 v[110:111], v[46:47]
	v_mov_b64_e32 v[114:115], v[50:51]
	v_mov_b64_e32 v[150:151], v[38:39]
	v_mov_b64_e32 v[154:155], v[42:43]
	v_mov_b64_e32 v[158:159], v[38:39]
	v_mov_b64_e32 v[162:163], v[42:43]
	v_mov_b64_e32 v[166:167], v[38:39]
	v_mov_b64_e32 v[170:171], v[42:43]
	v_mov_b64_e32 v[174:175], v[38:39]
	v_mov_b64_e32 v[178:179], v[42:43]
	s_mov_b32 s24, s14
	s_mov_b32 s23, s16
	s_mov_b64 s[20:21], 0
	s_mov_b32 s25, -2
	s_mov_b64 s[12:13], 0
	v_mov_b64_e32 v[52:53], v[44:45]
	v_mov_b64_e32 v[56:57], v[48:49]
	v_mov_b64_e32 v[60:61], v[44:45]
	v_mov_b64_e32 v[64:65], v[48:49]
	v_mov_b64_e32 v[68:69], v[44:45]
	v_mov_b64_e32 v[72:73], v[48:49]
	v_mov_b64_e32 v[76:77], v[44:45]
	v_mov_b64_e32 v[80:81], v[48:49]
	v_mov_b64_e32 v[116:117], v[36:37]
	v_mov_b64_e32 v[120:121], v[40:41]
	v_mov_b64_e32 v[124:125], v[36:37]
	v_mov_b64_e32 v[128:129], v[40:41]
	v_mov_b64_e32 v[132:133], v[36:37]
	v_mov_b64_e32 v[136:137], v[40:41]
	v_mov_b64_e32 v[140:141], v[36:37]
	v_mov_b64_e32 v[144:145], v[40:41]
	v_mov_b64_e32 v[84:85], v[44:45]
	v_mov_b64_e32 v[88:89], v[48:49]
	v_mov_b64_e32 v[92:93], v[44:45]
	v_mov_b64_e32 v[96:97], v[48:49]
	v_mov_b64_e32 v[100:101], v[44:45]
	v_mov_b64_e32 v[104:105], v[48:49]
	v_mov_b64_e32 v[108:109], v[44:45]
	v_mov_b64_e32 v[112:113], v[48:49]
	v_mov_b64_e32 v[148:149], v[36:37]
	v_mov_b64_e32 v[152:153], v[40:41]
	v_mov_b64_e32 v[156:157], v[36:37]
	v_mov_b64_e32 v[160:161], v[40:41]
	v_mov_b64_e32 v[164:165], v[36:37]
	v_mov_b64_e32 v[168:169], v[40:41]
	v_mov_b64_e32 v[172:173], v[36:37]
	v_mov_b64_e32 v[176:177], v[40:41]
	s_branch .LBB0_259

.LBB0_418:
	v_readlane_b32 s4, v254, 7
	s_lshl_b32 s82, s4, 6
	s_lshl_b64 s[2:3], s[82:83], 2
	s_add_u32 s2, s0, s2
	s_addc_u32 s3, s1, s3
	s_add_u32 s10, s2, 0xc800
	s_addc_u32 s11, s3, 0
	s_add_u32 s12, s58, 0x4100
	v_cvt_f32_u32_e32 v2, s4
	s_addc_u32 s13, s59, 0
	s_lshl_b32 s60, s4, 5
	s_add_u32 s56, s0, 0x126a2000
	v_readlane_b32 s5, v254, 8
	s_addc_u32 s57, s1, 0
	s_mov_b32 s2, s4
	s_add_u32 s54, s0, 0x26a2000
	s_mov_b32 s5, s83
	v_writelane_b32 v254, s2, 7
	v_mul_f32_e32 v2, 0xbe99999a, v2
	s_addc_u32 s55, s1, 0
	v_writelane_b32 v254, s3, 8
	s_lshl_b64 s[2:3], s[4:5], 2
	v_mul_f32_e32 v4, 0x3fb8aa3b, v2
	s_mov_b32 s4, 0x3fb8aa3b
	v_fma_f32 v5, v2, s4, -v4
	v_rndne_f32_e32 v6, v4
	v_fmac_f32_e32 v5, 0x32a5705f, v2
	v_sub_f32_e32 v4, v4, v6
	v_add_f32_e32 v4, v4, v5
	v_exp_f32_e32 v4, v4
	v_cvt_i32_f32_e32 v5, v6
	s_add_u32 s2, s0, s2
	s_addc_u32 s3, s1, s3
	s_add_u32 s20, s2, 0x6400
	s_mov_b32 s2, 0xc2ce8ed0
	v_ldexp_f32 v4, v4, v5
	v_cmp_ngt_f32_e32 vcc, s2, v2
	s_mov_b32 s2, 0x42b17218
	s_addc_u32 s21, s3, 0
	v_cndmask_b32_e32 v4, 0, v4, vcc
	v_cmp_nlt_f32_e32 vcc, s2, v2
	v_mov_b32_e32 v2, 0x7f800000
	s_add_u32 s24, s0, 0x42ac2000
	v_cndmask_b32_e32 v2, v2, v4, vcc
	v_mov_b32_e32 v4, 0xbf4ccccd
	v_fmamk_f32 v2, v2, 0x3f19999a, v4
	v_add_f32_e32 v147, 1.0, v2
	s_addc_u32 s25, s1, 0
	v_cmp_eq_u32_e32 vcc, 0, v0
	s_and_saveexec_b64 s[84:85], vcc
	s_cbranch_execz .Ldif_tk_skip
	v_mov_b32_e32 v218, 1
	v_mov_b32_e32 v219, 1
	global_atomic_add v218, v3, v218, s[12:13] sc0
	global_atomic_add v219, v3, v219, s[10:11] sc0
.Ldif_tk_skip:
	s_or_b64 exec, exec, s[84:85]
	s_branch .LBB0_420
.LBB0_419:
	s_and_b64 vcc, exec, s[34:35]
	s_cbranch_vccnz .LBB0_485
.LBB0_420:
	s_setprio 0
	v_mov_b32_e32 v2, v0
	s_barrier
	s_nop 0
	v_cmp_eq_u32_e32 vcc, 0, v2
	s_and_saveexec_b64 s[2:3], vcc
	s_cbranch_execz .LBB0_426
	s_waitcnt vmcnt(0)
	v_mov_b32_e32 v6, v218
	v_min_u32_e32 v7, 0xc00, v219
	v_mov_b32_e32 v2, s73
	ds_write_b64 v2, v[6:7]
	v_cmp_gt_u32_e32 vcc, 0x400, v6
	s_and_saveexec_b64 s[4:5], vcc
	s_cbranch_execz .Ldif_tk_nomore
	v_mov_b32_e32 v218, 1
	v_mov_b32_e32 v219, 1
	global_atomic_add v218, v3, v218, s[12:13] sc0
	global_atomic_add v219, v3, v219, s[10:11] sc0
.Ldif_tk_nomore:
	s_or_b64 exec, exec, s[4:5]
.LBB0_426:
	s_or_b64 exec, exec, s[2:3]
	v_mov_b32_e32 v2, s73
	s_waitcnt lgkmcnt(0)
	s_barrier
	s_waitcnt vmcnt(7)
	ds_read_b64 v[4:5], v2
	s_waitcnt lgkmcnt(0)
	v_readfirstlane_b32 s33, v4
	s_cmpk_gt_i32 s33, 0x3ff
	s_cselect_b64 s[34:35], -1, 0
	s_cmpk_lt_i32 s33, 0x400
	v_readfirstlane_b32 s61, v5
	s_cbranch_scc1 .LBB0_432
	s_mov_b64 s[4:5], 0
	s_cmpk_lt_i32 s61, 0xc00
	s_mov_b64 s[38:39], 0
	s_cbranch_scc0 .LBB0_433
	s_mul_hi_i32 s2, s61, 0x2aaaaaab
	s_lshr_b32 s3, s2, 31
	s_ashr_i32 s2, s2, 4
	s_add_i32 s14, s2, s3
	s_mul_i32 s16, s14, 0xffffffa0
	s_add_i32 s16, s16, s61
	v_mov_b32_e32 v38, v0
	s_cmp_gt_i32 s16, 63
	s_cselect_b64 s[2:3], -1, 0
	s_add_i32 s36, s14, s60
	s_lshl_b32 s14, s61, 7
	v_ashrrev_i32_e32 v2, 2, v38
	s_and_b32 s62, s14, 0x380
	v_and_b32_e32 v2, -4, v2
	v_add_u32_e32 v6, s62, v2
	s_ashr_i32 s37, s36, 31
	v_ashrrev_i32_e32 v7, 31, v6
	s_mov_b64 s[14:15], -1
	s_and_b64 vcc, exec, s[2:3]
	s_cbranch_vccz .LBB0_430
	s_load_dwordx2 s[14:15], s[6:7], 0xb0
	s_lshl_b64 s[18:19], s[36:37], 22
	v_lshlrev_b64 v[4:5], 12, v[6:7]
	s_waitcnt lgkmcnt(0)
	s_add_u32 s14, s14, s18
	s_addc_u32 s15, s15, s19
	s_lshl_b32 s17, s16, 5
	s_and_b32 s63, s17, 0xffffff00
	v_lshl_add_u64 v[4:5], s[14:15], 0, v[4:5]
	s_add_i32 s82, s63, 0xfffff800
	v_lshl_add_u64 v[4:5], s[82:83], 2, v[4:5]
	s_mov_b64 s[14:15], 0

.LBB0_681:
	s_flbit_i32_b32 s0, s2
	s_xor_b32 s0, s0, 31
	s_lshl_b32 s8, 1, s0
	s_waitcnt lgkmcnt(0)
	v_and_b32_e32 v2, s8, v136
	v_cmp_ne_u32_e64 s[38:39], 0, v2
	s_mov_b64 vcc, s[38:39]
	s_cbranch_vccz .LBB0_669
	s_and_b32 s1, s5, 0xc000
	s_lshl_b32 s9, s0, 6
	s_lshr_b32 s0, s0, 2
	s_xor_b32 s1, s1, 0x8000
	v_cvt_f32_u32_e32 v159, s0
	s_add_i32 s1, s1, 0
	v_add_u32_e32 v2, s1, v137
	v_add_u32_e32 v4, s1, v138
	v_add_u32_e32 v5, s1, v139
	v_add_u32_e32 v6, s1, v140
	s_or_b32 s10, s9, 32
	s_cmp_gt_i32 s10, s6
	v_add_u32_e32 v163, v2, v134
	v_add_u32_e32 v162, v4, v134
	v_add_u32_e32 v161, v5, v134
	v_add_u32_e32 v160, v6, v134
	v_add_u32_e32 v17, s1, v156
	v_add_u32_e32 v16, s1, v157
	s_cbranch_scc1 .LBB0_690
	ds_read_b128 v[4:7], v163 offset:4096
	ds_read_b128 v[188:191], v162 offset:4096
	ds_read_b128 v[192:195], v161 offset:4096
	ds_read_b128 v[202:205], v160 offset:4096
	s_and_b32 s0, s10, 0xe0
	v_or_b32_e32 v2, s0, v129
	v_cvt_f32_ubyte0_e32 v2, v2
	v_and_b32_e32 v2, 0x7fff0000, v2
	v_or_b32_sdwa v2, v2, v159 dst_sel:DWORD dst_unused:UNUSED_PAD src0_sel:DWORD src1_sel:WORD_1
	v_cndmask_b32_e64 v2, 0, v2, s[22:23]
	s_or_b32 s0, s9, 63
	s_cmp_lt_u32 s16, s0
	s_waitcnt lgkmcnt(3)
	v_mfma_f32_32x32x16_bf16 v[82:97], v[4:7], v[106:109], 0
	s_cselect_b64 s[0:1], -1, 0
	s_sub_i32 s11, s16, s10
	s_cmp_gt_i32 s11, 0x3fffffe0
	v_add3_u32 v164, v16, v135, s69
	s_cselect_b64 s[12:13], -1, 0
	s_or_b64 s[0:1], s[0:1], s[12:13]
	s_and_b64 vcc, exec, s[0:1]
	s_waitcnt lgkmcnt(2)
	v_mfma_f32_32x32x16_bf16 v[82:97], v[188:191], v[98:101], v[82:97]
	s_waitcnt lgkmcnt(1)
	v_mfma_f32_32x32x16_bf16 v[82:97], v[192:195], v[102:105], v[82:97]
	s_waitcnt lgkmcnt(0)
	v_mfma_f32_32x32x16_bf16 v[82:97], v[202:205], v[110:113], v[82:97]
	v_mov_b32_e32 v4, v3
	v_mov_b32_e32 v5, v3
	s_nop 1
	v_mfma_f32_32x32x16_bf16 v[82:97], v[2:5], v[114:117], v[82:97]
	v_add3_u32 v2, v17, v135, s69
	ds_read_b64_tr_b16 v[118:119], v2
	ds_read_b64_tr_b16 v[120:121], v2 offset:1024
	ds_read_b64_tr_b16 v[12:13], v164
	ds_read_b64_tr_b16 v[14:15], v164 offset:1024
	ds_read_b64_tr_b16 v[8:9], v2 offset:2048
	ds_read_b64_tr_b16 v[10:11], v2 offset:3072
	ds_read_b64_tr_b16 v[4:5], v164 offset:2048
	ds_read_b64_tr_b16 v[6:7], v164 offset:3072
	s_cbranch_vccnz .LBB0_685
	v_cndmask_b32_e64 v2, 0, 1, s[38:39]
	v_cmp_ne_u32_e32 vcc, 0, v2
	s_cmp_lg_u64 vcc, exec
	s_cselect_b64 s[0:1], -1, 0
	s_cbranch_scc0 .LBB0_687
	v_cndmask_b32_e64 v82, v197, v82, s[38:39]
	v_cndmask_b32_e64 v83, v197, v83, s[38:39]
	v_cndmask_b32_e64 v84, v197, v84, s[38:39]
	v_cndmask_b32_e64 v85, v197, v85, s[38:39]
	v_cndmask_b32_e64 v86, v197, v86, s[38:39]
	v_cndmask_b32_e64 v87, v197, v87, s[38:39]
	v_cndmask_b32_e64 v88, v197, v88, s[38:39]
	v_cndmask_b32_e64 v89, v197, v89, s[38:39]
	v_cndmask_b32_e64 v90, v197, v90, s[38:39]
	v_cndmask_b32_e64 v91, v197, v91, s[38:39]
	v_cndmask_b32_e64 v92, v197, v92, s[38:39]
	v_cndmask_b32_e64 v93, v197, v93, s[38:39]
	v_cndmask_b32_e64 v94, v197, v94, s[38:39]
	v_cndmask_b32_e64 v95, v197, v95, s[38:39]
	v_cndmask_b32_e64 v96, v197, v96, s[38:39]
	v_cndmask_b32_e64 v97, v197, v97, s[38:39]
	s_branch .LBB0_687

.LBB0_690:
	s_cmp_gt_i32 s9, s6
	s_cbranch_scc1 .LBB0_669
	ds_read_b128 v[4:7], v163
	ds_read_b128 v[188:191], v162
	ds_read_b128 v[192:195], v161
	ds_read_b128 v[202:205], v160
	s_and_b32 s0, s9, 0xc0
	v_or_b32_e32 v2, s0, v129
	v_cvt_f32_ubyte0_e32 v2, v2
	v_and_b32_e32 v2, 0x7fff0000, v2
	v_or_b32_sdwa v2, v2, v159 dst_sel:DWORD dst_unused:UNUSED_PAD src0_sel:DWORD src1_sel:WORD_1
	v_cndmask_b32_e64 v2, 0, v2, s[22:23]
	s_or_b32 s0, s9, 31
	s_cmp_lt_i32 s16, s0
	s_waitcnt lgkmcnt(3)
	v_mfma_f32_32x32x16_bf16 v[82:97], v[4:7], v[106:109], 0
	s_cselect_b64 s[0:1], -1, 0
	s_sub_i32 s10, s16, s9
	s_cmp_gt_i32 s10, 0x3fffffe0
	v_add3_u32 v16, v16, v135, s67
	s_cselect_b64 s[10:11], -1, 0
	s_or_b64 s[0:1], s[0:1], s[10:11]
	s_and_b64 vcc, exec, s[0:1]
	s_waitcnt lgkmcnt(2)
	v_mfma_f32_32x32x16_bf16 v[82:97], v[188:191], v[98:101], v[82:97]
	s_waitcnt lgkmcnt(1)
	v_mfma_f32_32x32x16_bf16 v[82:97], v[192:195], v[102:105], v[82:97]
	s_waitcnt lgkmcnt(0)
	v_mfma_f32_32x32x16_bf16 v[82:97], v[202:205], v[110:113], v[82:97]
	v_mov_b32_e32 v4, v3
	v_mov_b32_e32 v5, v3
	s_nop 1
	v_mfma_f32_32x32x16_bf16 v[82:97], v[2:5], v[114:117], v[82:97]
	v_add3_u32 v2, v17, v135, s67
	ds_read_b64_tr_b16 v[118:119], v2
	ds_read_b64_tr_b16 v[120:121], v2 offset:1024
	ds_read_b64_tr_b16 v[12:13], v16
	ds_read_b64_tr_b16 v[14:15], v16 offset:1024
	ds_read_b64_tr_b16 v[8:9], v2 offset:2048
	ds_read_b64_tr_b16 v[10:11], v2 offset:3072
	ds_read_b64_tr_b16 v[4:5], v16 offset:2048
	ds_read_b64_tr_b16 v[6:7], v16 offset:3072
	s_cbranch_vccnz .LBB0_693
	v_cndmask_b32_e64 v2, 0, 1, s[38:39]
	v_cmp_ne_u32_e32 vcc, 0, v2
	s_cmp_lg_u64 vcc, exec
	s_cselect_b64 s[0:1], -1, 0
	s_cbranch_scc0 .LBB0_695
	v_cndmask_b32_e64 v82, v197, v82, s[38:39]
	v_cndmask_b32_e64 v83, v197, v83, s[38:39]
	v_cndmask_b32_e64 v84, v197, v84, s[38:39]
	v_cndmask_b32_e64 v85, v197, v85, s[38:39]
	v_cndmask_b32_e64 v86, v197, v86, s[38:39]
	v_cndmask_b32_e64 v87, v197, v87, s[38:39]
	v_cndmask_b32_e64 v88, v197, v88, s[38:39]
	v_cndmask_b32_e64 v89, v197, v89, s[38:39]
	v_cndmask_b32_e64 v90, v197, v90, s[38:39]
	v_cndmask_b32_e64 v91, v197, v91, s[38:39]
	v_cndmask_b32_e64 v92, v197, v92, s[38:39]
	v_cndmask_b32_e64 v93, v197, v93, s[38:39]
	v_cndmask_b32_e64 v94, v197, v94, s[38:39]
	v_cndmask_b32_e64 v95, v197, v95, s[38:39]
	v_cndmask_b32_e64 v96, v197, v96, s[38:39]
	v_cndmask_b32_e64 v97, v197, v97, s[38:39]
	s_branch .LBB0_695

.LBB0_1247:
	s_lshl_b32 s2, s17, 2
	s_add_i32 s29, s2, 0
	s_waitcnt vmcnt(4)
	v_mov_b64_e32 v[54:55], v[46:47]
	v_mov_b64_e32 v[62:63], v[50:51]
	v_mov_b64_e32 v[70:71], v[46:47]
	v_mov_b64_e32 v[78:79], v[50:51]
	v_mov_b64_e32 v[86:87], v[46:47]
	v_mov_b64_e32 v[94:95], v[50:51]
	v_mov_b64_e32 v[102:103], v[46:47]
	v_mov_b64_e32 v[110:111], v[50:51]
	v_mov_b64_e32 v[58:59], v[38:39]
	v_mov_b64_e32 v[66:67], v[42:43]
	v_mov_b64_e32 v[74:75], v[38:39]
	v_mov_b64_e32 v[82:83], v[42:43]
	v_mov_b64_e32 v[90:91], v[38:39]
	v_mov_b64_e32 v[98:99], v[42:43]
	v_mov_b64_e32 v[106:107], v[38:39]
	v_mov_b64_e32 v[114:115], v[42:43]
	v_mov_b64_e32 v[118:119], v[46:47]
	v_mov_b64_e32 v[126:127], v[50:51]
	v_mov_b64_e32 v[134:135], v[46:47]
	v_mov_b64_e32 v[142:143], v[50:51]
	v_mov_b64_e32 v[150:151], v[46:47]
	v_mov_b64_e32 v[158:159], v[50:51]
	v_mov_b64_e32 v[166:167], v[46:47]
	v_mov_b64_e32 v[174:175], v[50:51]
	v_mov_b64_e32 v[122:123], v[38:39]
	v_mov_b64_e32 v[130:131], v[42:43]
	v_mov_b64_e32 v[138:139], v[38:39]
	v_mov_b64_e32 v[146:147], v[42:43]
	v_mov_b64_e32 v[154:155], v[38:39]
	v_mov_b64_e32 v[162:163], v[42:43]
	v_mov_b64_e32 v[170:171], v[38:39]
	v_mov_b64_e32 v[178:179], v[42:43]
	s_add_i32 s27, s29, 0x21004
	s_add_i32 s28, s17, 1
	s_add_i32 s29, s29, 0x21000
	s_mov_b32 s30, 0
	s_mov_b64 s[12:13], 0
	v_mov_b64_e32 v[52:53], v[44:45]
	v_mov_b64_e32 v[60:61], v[48:49]
	v_mov_b64_e32 v[68:69], v[44:45]
	v_mov_b64_e32 v[76:77], v[48:49]
	v_mov_b64_e32 v[84:85], v[44:45]
	v_mov_b64_e32 v[92:93], v[48:49]
	v_mov_b64_e32 v[100:101], v[44:45]
	v_mov_b64_e32 v[108:109], v[48:49]
	v_mov_b64_e32 v[56:57], v[36:37]
	v_mov_b64_e32 v[64:65], v[40:41]
	v_mov_b64_e32 v[72:73], v[36:37]
	v_mov_b64_e32 v[80:81], v[40:41]
	v_mov_b64_e32 v[88:89], v[36:37]
	v_mov_b64_e32 v[96:97], v[40:41]
	v_mov_b64_e32 v[104:105], v[36:37]
	v_mov_b64_e32 v[112:113], v[40:41]
	v_mov_b64_e32 v[116:117], v[44:45]
	v_mov_b64_e32 v[124:125], v[48:49]
	v_mov_b64_e32 v[132:133], v[44:45]
	v_mov_b64_e32 v[140:141], v[48:49]
	v_mov_b64_e32 v[148:149], v[44:45]
	v_mov_b64_e32 v[156:157], v[48:49]
	v_mov_b64_e32 v[164:165], v[44:45]
	v_mov_b64_e32 v[172:173], v[48:49]
	v_mov_b64_e32 v[120:121], v[36:37]
	v_mov_b64_e32 v[128:129], v[40:41]
	v_mov_b64_e32 v[136:137], v[36:37]
	v_mov_b64_e32 v[144:145], v[40:41]
	v_mov_b64_e32 v[152:153], v[36:37]
	v_mov_b64_e32 v[160:161], v[40:41]
	v_mov_b64_e32 v[168:169], v[36:37]
	v_mov_b64_e32 v[176:177], v[40:41]

.LBB0_1386:
	s_mov_b32 s2, 0x41800000
	s_waitcnt vmcnt(8)
	v_pk_mul_f32 v[102:103], v[248:249], s[2:3] op_sel_hi:[1,0]
	v_pk_mul_f32 v[100:101], v[246:247], s[2:3] op_sel_hi:[1,0]
	v_pk_mul_f32 v[106:107], v[194:195], s[2:3] op_sel_hi:[1,0]
	v_pk_mul_f32 v[104:105], v[192:193], s[2:3] op_sel_hi:[1,0]
	v_pk_mul_f32 v[54:55], v[50:51], s[2:3] op_sel_hi:[1,0]
	v_pk_mul_f32 v[52:53], v[48:49], s[2:3] op_sel_hi:[1,0]
	v_pk_mul_f32 v[58:59], v[46:47], s[2:3] op_sel_hi:[1,0]
	v_pk_mul_f32 v[56:57], v[44:45], s[2:3] op_sel_hi:[1,0]
	s_lshl_b32 s2, s15, 2
	s_add_i32 s22, s2, 0
	v_mov_b64_e32 v[62:63], v[58:59]
	v_mov_b64_e32 v[66:67], v[54:55]
	v_mov_b64_e32 v[70:71], v[58:59]
	v_mov_b64_e32 v[74:75], v[54:55]
	v_mov_b64_e32 v[78:79], v[58:59]
	v_mov_b64_e32 v[82:83], v[54:55]
	v_mov_b64_e32 v[126:127], v[106:107]
	v_mov_b64_e32 v[130:131], v[102:103]
	v_mov_b64_e32 v[134:135], v[106:107]
	v_mov_b64_e32 v[138:139], v[102:103]
	v_mov_b64_e32 v[142:143], v[106:107]
	v_mov_b64_e32 v[146:147], v[102:103]
	v_mov_b64_e32 v[86:87], v[58:59]
	v_mov_b64_e32 v[90:91], v[54:55]
	v_mov_b64_e32 v[94:95], v[58:59]
	v_mov_b64_e32 v[98:99], v[54:55]
	v_mov_b64_e32 v[110:111], v[58:59]
	v_mov_b64_e32 v[114:115], v[54:55]
	v_mov_b64_e32 v[118:119], v[58:59]
	v_mov_b64_e32 v[122:123], v[54:55]
	v_mov_b64_e32 v[150:151], v[106:107]
	v_mov_b64_e32 v[154:155], v[102:103]
	v_mov_b64_e32 v[158:159], v[106:107]
	v_mov_b64_e32 v[162:163], v[102:103]
	v_mov_b64_e32 v[166:167], v[106:107]
	v_mov_b64_e32 v[170:171], v[102:103]
	v_mov_b64_e32 v[174:175], v[106:107]
	v_mov_b64_e32 v[178:179], v[102:103]
	s_add_i32 s20, s22, 0x21004
	s_add_i32 s21, s15, 1
	s_add_i32 s22, s22, 0x21000
	s_mov_b32 s23, 0
	s_mov_b64 s[10:11], 0
	v_mov_b64_e32 v[60:61], v[56:57]
	v_mov_b64_e32 v[64:65], v[52:53]
	v_mov_b64_e32 v[68:69], v[56:57]
	v_mov_b64_e32 v[72:73], v[52:53]
	v_mov_b64_e32 v[76:77], v[56:57]
	v_mov_b64_e32 v[80:81], v[52:53]
	v_mov_b64_e32 v[124:125], v[104:105]
	v_mov_b64_e32 v[128:129], v[100:101]
	v_mov_b64_e32 v[132:133], v[104:105]
	v_mov_b64_e32 v[136:137], v[100:101]
	v_mov_b64_e32 v[140:141], v[104:105]
	v_mov_b64_e32 v[144:145], v[100:101]
	v_mov_b64_e32 v[84:85], v[56:57]
	v_mov_b64_e32 v[88:89], v[52:53]
	v_mov_b64_e32 v[92:93], v[56:57]
	v_mov_b64_e32 v[96:97], v[52:53]
	v_mov_b64_e32 v[108:109], v[56:57]
	v_mov_b64_e32 v[112:113], v[52:53]
	v_mov_b64_e32 v[116:117], v[56:57]
	v_mov_b64_e32 v[120:121], v[52:53]
	v_mov_b64_e32 v[148:149], v[104:105]
	v_mov_b64_e32 v[152:153], v[100:101]
	v_mov_b64_e32 v[156:157], v[104:105]
	v_mov_b64_e32 v[160:161], v[100:101]
	v_mov_b64_e32 v[164:165], v[104:105]
	v_mov_b64_e32 v[168:169], v[100:101]
	v_mov_b64_e32 v[172:173], v[104:105]
	v_mov_b64_e32 v[176:177], v[100:101]
